# b7 + exp2: next tile's slot-weight table touched into cache during the K loop (epilogue loads hit)
# baseline (speedup 1.0000x reference)
.LBB0_3603:
	v_readlane_b32 s0, v255, 0
	v_readlane_b32 s1, v255, 1
	s_andn2_b64 vcc, exec, s[0:1]
	s_cbranch_vccnz .LBB0_3649
	s_mov_b32 s3, s40
	s_lshl_b64 s[0:1], s[2:3], 2
	v_readlane_b32 s2, v254, 58
	v_readlane_b32 s3, v254, 59
	s_add_u32 s33, s2, s0
	s_mov_b32 s43, s40
	s_addc_u32 s36, s3, s1
	s_lshl_b64 s[0:1], s[42:43], 3
	v_readlane_b32 s2, v255, 4
	v_readlane_b32 s3, v255, 5
	s_add_u32 s0, s2, s0
	s_addc_u32 s1, s3, s1
	s_lshl_b32 s4, s81, 3
	s_cmp_lt_i32 s92, s4
	s_cselect_b64 s[2:3], -1, 0
	v_writelane_b32 v254, s2, 42
	s_nop 1
	v_writelane_b32 v254, s3, 43
	s_mov_b32 s2, 0
	v_readlane_b32 s3, v254, 40
	s_cmp_lt_i32 s3, s81
	s_cselect_b64 s[8:9], -1, 0
	v_writelane_b32 v254, s8, 44
	s_nop 1
	v_writelane_b32 v254, s9, 45
	v_mbcnt_lo_u32_b32 v242, -1, 0
	v_mbcnt_hi_u32_b32 v242, -1, v242
	s_and_b32 s8, s92, 7
	s_lshl_b32 s8, s8, 2
	s_bfe_u32 s9, s92, 0x20003
	s_add_i32 s8, s8, s9
	v_lshl_add_u32 v242, v242, 5, s8
	v_lshlrev_b32_e32 v242, 2, v242
	s_mov_b32 s8, s33
	s_mov_b32 s9, s36
	s_nop 0
	global_load_dword v242, v242, s[8:9]
	s_waitcnt vmcnt(0)
	v_mbcnt_lo_u32_b32 v243, -1, 0
	v_mbcnt_hi_u32_b32 v243, -1, v243
	v_lshlrev_b32_e32 v243, 4, v243
	s_nop 0
	s_nop 0
	s_nop 0
	s_nop 0
	s_nop 0
	s_nop 0
	s_nop 0
	s_nop 0
	s_nop 0
	s_nop 0
	s_nop 0
	s_nop 0
	s_nop 0
	s_nop 0
	s_nop 0
	s_nop 0
	s_nop 0
	s_nop 0
	s_nop 0
	s_nop 0
	s_nop 0
	s_nop 0
	s_nop 0
	s_nop 0
	s_nop 0
	s_branch .LBB0_3607

.LBB0_3625:
	s_ashr_i32 s23, s22, 31
	s_lshl_b64 s[26:27], s[22:23], 17
	s_add_u32 s34, s66, s26
	s_addc_u32 s35, s67, s27
	s_and_b64 s[26:27], s[16:17], exec
	s_cselect_b32 s29, s35, s19
	s_cselect_b32 s28, s34, s18
	s_lshl_b32 s26, s60, 8
	s_ashr_i32 s25, s24, 31
	s_ashr_i32 s27, s26, 31
	s_lshl_b64 s[30:31], s[24:25], 20
	s_lshl_b64 s[26:27], s[26:27], 9
	s_add_u32 s13, s39, s30
	s_addc_u32 s23, s80, s31
	s_add_u32 s30, s13, s26
	s_addc_u32 s31, s23, s27
	s_and_b64 s[26:27], s[16:17], exec
	s_cselect_b32 s27, s31, s21
	s_cselect_b32 s26, s30, s20
	s_add_i32 s23, 0, 0x10000
	v_add_u32_e32 v142, s23, v215
	ds_read_b128 v[6:9], v142
	ds_read_b128 v[10:13], v142 offset:1024
	s_waitcnt vmcnt(0)
	v_mov_b32_e32 v252, s22
	v_lshl_add_u32 v252, v252, 11, v243
	global_load_dwordx4 v[244:247], v252, s[0:1]
	global_load_dwordx4 v[248:251], v252, s[0:1] offset:1024
	s_nop 0
	s_nop 0
	s_nop 0
	s_nop 0
	s_nop 0
	s_nop 0
	s_nop 0
	s_nop 0
	s_nop 0
	ds_read_b128 v[164:167], v142 offset:2048
	ds_read_b128 v[168:171], v142 offset:3072
	s_mov_b64 vcc, -1
	v_lshl_add_u64 v[130:131], s[18:19], 0, v[154:155]
	s_add_i32 s61, s15, 0xc000
	v_lshl_add_u64 v[2:3], v[130:131], 0, s[44:45]
	s_mov_b32 m0, s61
	v_lshl_add_u64 v[132:133], s[18:19], 0, v[156:157]
	s_add_i32 s13, s15, 0xe000
	ds_read_b128 v[14:17], v217
	ds_read_b128 v[18:21], v217 offset:1024
	ds_read_b128 v[22:25], v217 offset:2048
	ds_read_b128 v[26:29], v217 offset:3072
	ds_read_b128 v[30:33], v217 offset:4096
	ds_read_b128 v[34:37], v217 offset:5120
	ds_read_b128 v[38:41], v217 offset:6144
	ds_read_b128 v[42:45], v217 offset:7168
	global_load_lds_dwordx4 v[2:3], off
	v_lshl_add_u64 v[2:3], v[132:133], 0, s[44:45]
	s_mov_b32 m0, s13
	s_nop 0
	global_load_lds_dwordx4 v[2:3], off
	s_waitcnt lgkmcnt(8)
	s_barrier
	s_waitcnt lgkmcnt(0)
	s_setprio 1
	s_mov_b32 s41, s40
	s_mov_b32 s42, s40
	s_mov_b32 s43, s40
	v_mov_b64_e32 v[2:3], s[40:41]
	v_mov_b64_e32 v[120:121], s[42:43]
	v_mov_b64_e32 v[116:117], s[42:43]
	v_mov_b64_e32 v[104:105], s[42:43]
	v_mov_b64_e32 v[100:101], s[42:43]
	v_mov_b64_e32 v[88:89], s[42:43]
	v_mov_b64_e32 v[84:85], s[42:43]
	v_mov_b64_e32 v[60:61], s[42:43]
	v_mov_b64_e32 v[52:53], s[42:43]
	v_mov_b64_e32 v[4:5], s[42:43]
	v_mov_b64_e32 v[118:119], s[40:41]
	v_mov_b64_e32 v[114:115], s[40:41]
	v_mov_b64_e32 v[102:103], s[40:41]
	v_mov_b64_e32 v[98:99], s[40:41]
	v_mov_b64_e32 v[86:87], s[40:41]
	v_mov_b64_e32 v[82:83], s[40:41]
	v_mov_b64_e32 v[58:59], s[40:41]
	v_mov_b64_e32 v[50:51], s[40:41]
	s_waitcnt lgkmcnt(0)
	v_mfma_scale_f32_16x16x128_f8f6f4 v[118:121], v[6:13], v[14:21], v[118:121], v210, v210 op_sel_hi:[0,0,0]
	v_mfma_scale_f32_16x16x128_f8f6f4 v[114:117], v[164:171], v[14:21], v[114:117], v210, v210 op_sel_hi:[0,0,0]
	v_mfma_scale_f32_16x16x128_f8f6f4 v[102:105], v[6:13], v[22:29], v[102:105], v210, v210 op_sel_hi:[0,0,0]
	v_mfma_scale_f32_16x16x128_f8f6f4 v[98:101], v[164:171], v[22:29], v[98:101], v210, v210 op_sel_hi:[0,0,0]
	v_mfma_scale_f32_16x16x128_f8f6f4 v[86:89], v[6:13], v[30:37], v[86:89], v210, v210 op_sel_hi:[0,0,0]
	v_mfma_scale_f32_16x16x128_f8f6f4 v[82:85], v[164:171], v[30:37], v[82:85], v210, v210 op_sel_hi:[0,0,0]
	v_mfma_scale_f32_16x16x128_f8f6f4 v[58:61], v[6:13], v[38:45], v[58:61], v210, v210 op_sel_hi:[0,0,0]
	v_mfma_scale_f32_16x16x128_f8f6f4 v[50:53], v[164:171], v[38:45], v[50:53], v210, v210 op_sel_hi:[0,0,0]
	s_setprio 0
	s_barrier
	s_add_i32 s25, 0, 0x14000
	v_lshl_add_u64 v[134:135], s[20:21], 0, v[146:147]
	s_add_i32 s41, s23, s87
	v_add_u32_e32 v143, s25, v215
	v_lshl_add_u64 v[46:47], v[134:135], 0, s[84:85]
	s_mov_b32 m0, s41
	v_lshl_add_u64 v[136:137], s[20:21], 0, v[148:149]
	s_add_i32 s23, s41, 0x2000
	ds_read_b128 v[172:175], v143
	ds_read_b128 v[176:179], v143 offset:1024
	ds_read_b128 v[180:183], v143 offset:2048
	ds_read_b128 v[184:187], v143 offset:3072
	global_load_lds_dwordx4 v[46:47], off
	v_lshl_add_u64 v[46:47], v[136:137], 0, s[84:85]
	s_mov_b32 m0, s23
	s_nop 0
	global_load_lds_dwordx4 v[46:47], off
	s_barrier
	s_waitcnt lgkmcnt(0)
	s_setprio 1
	v_mov_b64_e32 v[128:129], v[4:5]
	v_mov_b64_e32 v[124:125], v[4:5]
	v_mov_b64_e32 v[112:113], v[4:5]
	v_mov_b64_e32 v[108:109], v[4:5]
	v_mov_b64_e32 v[96:97], v[4:5]
	v_mov_b64_e32 v[92:93], v[4:5]
	v_mov_b64_e32 v[80:81], v[4:5]
	v_mov_b64_e32 v[76:77], v[4:5]
	v_mov_b64_e32 v[126:127], v[2:3]
	v_mov_b64_e32 v[122:123], v[2:3]
	v_mov_b64_e32 v[110:111], v[2:3]
	v_mov_b64_e32 v[106:107], v[2:3]
	v_mov_b64_e32 v[94:95], v[2:3]
	v_mov_b64_e32 v[90:91], v[2:3]
	v_mov_b64_e32 v[78:79], v[2:3]
	v_mov_b64_e32 v[74:75], v[2:3]
	s_waitcnt lgkmcnt(0)
	v_mfma_scale_f32_16x16x128_f8f6f4 v[126:129], v[172:179], v[14:21], v[126:129], v210, v210 op_sel_hi:[0,0,0]
	v_mfma_scale_f32_16x16x128_f8f6f4 v[122:125], v[180:187], v[14:21], v[122:125], v210, v210 op_sel_hi:[0,0,0]
	v_mfma_scale_f32_16x16x128_f8f6f4 v[110:113], v[172:179], v[22:29], v[110:113], v210, v210 op_sel_hi:[0,0,0]
	v_mfma_scale_f32_16x16x128_f8f6f4 v[106:109], v[180:187], v[22:29], v[106:109], v210, v210 op_sel_hi:[0,0,0]
	v_mfma_scale_f32_16x16x128_f8f6f4 v[94:97], v[172:179], v[30:37], v[94:97], v210, v210 op_sel_hi:[0,0,0]
	v_mfma_scale_f32_16x16x128_f8f6f4 v[90:93], v[180:187], v[30:37], v[90:93], v210, v210 op_sel_hi:[0,0,0]
	v_mfma_scale_f32_16x16x128_f8f6f4 v[78:81], v[172:179], v[38:45], v[78:81], v210, v210 op_sel_hi:[0,0,0]
	v_mfma_scale_f32_16x16x128_f8f6f4 v[74:77], v[180:187], v[38:45], v[74:77], v210, v210 op_sel_hi:[0,0,0]
	s_setprio 0
	v_lshl_add_u64 v[138:139], s[18:19], 0, v[150:151]
	s_mov_b32 m0, s15
	v_lshl_add_u64 v[14:15], v[138:139], 0, s[84:85]
	v_lshl_add_u64 v[140:141], s[18:19], 0, v[152:153]
	s_barrier
	ds_read_b128 v[188:191], v217 offset:16384
	ds_read_b128 v[192:195], v217 offset:17408
	ds_read_b128 v[196:199], v217 offset:18432
	ds_read_b128 v[200:203], v217 offset:19456
	ds_read_b128 v[218:221], v217 offset:20480
	ds_read_b128 v[222:225], v217 offset:21504
	ds_read_b128 v[226:229], v217 offset:22528
	ds_read_b128 v[230:233], v217 offset:23552
	global_load_lds_dwordx4 v[14:15], off
	v_lshl_add_u64 v[14:15], v[140:141], 0, s[84:85]
	s_mov_b32 m0, s8
	s_nop 0
	global_load_lds_dwordx4 v[14:15], off
	s_barrier
	s_waitcnt lgkmcnt(0)
	s_setprio 1
	v_mov_b64_e32 v[72:73], v[4:5]
	v_mov_b64_e32 v[64:65], v[4:5]
	v_mov_b64_e32 v[48:49], v[4:5]
	v_mov_b64_e32 v[40:41], v[4:5]
	v_mov_b64_e32 v[32:33], v[4:5]
	v_mov_b64_e32 v[24:25], v[4:5]
	v_mov_b64_e32 v[16:17], v[4:5]
	v_mov_b64_e32 v[70:71], v[2:3]
	v_mov_b64_e32 v[62:63], v[2:3]
	v_mov_b64_e32 v[46:47], v[2:3]
	v_mov_b64_e32 v[38:39], v[2:3]
	v_mov_b64_e32 v[30:31], v[2:3]
	v_mov_b64_e32 v[22:23], v[2:3]
	v_mov_b64_e32 v[14:15], v[2:3]
	s_waitcnt lgkmcnt(0)
	v_mfma_scale_f32_16x16x128_f8f6f4 v[70:73], v[6:13], v[188:195], v[70:73], v210, v210 op_sel_hi:[0,0,0]
	v_mfma_scale_f32_16x16x128_f8f6f4 v[62:65], v[164:171], v[188:195], v[62:65], v210, v210 op_sel_hi:[0,0,0]
	v_mfma_scale_f32_16x16x128_f8f6f4 v[46:49], v[6:13], v[196:203], v[46:49], v210, v210 op_sel_hi:[0,0,0]
	v_mfma_scale_f32_16x16x128_f8f6f4 v[38:41], v[164:171], v[196:203], v[38:41], v210, v210 op_sel_hi:[0,0,0]
	v_mfma_scale_f32_16x16x128_f8f6f4 v[30:33], v[6:13], v[218:225], v[30:33], v210, v210 op_sel_hi:[0,0,0]
	v_mfma_scale_f32_16x16x128_f8f6f4 v[22:25], v[164:171], v[218:225], v[22:25], v210, v210 op_sel_hi:[0,0,0]
	v_mfma_scale_f32_16x16x128_f8f6f4 v[14:17], v[6:13], v[226:233], v[14:17], v210, v210 op_sel_hi:[0,0,0]
	v_mov_b64_e32 v[8:9], v[4:5]
	v_mov_b64_e32 v[6:7], v[2:3]
	v_mfma_scale_f32_16x16x128_f8f6f4 v[6:9], v[164:171], v[226:233], v[6:9], v210, v210 op_sel_hi:[0,0,0]
	s_setprio 0
	s_barrier
	s_add_u32 s42, s20, 0x10100
	s_addc_u32 s43, s21, 0
	s_add_i32 s19, s25, s87
	v_lshl_add_u64 v[10:11], s[42:43], 0, v[146:147]
	s_mov_b32 m0, s19
	s_add_i32 s18, s19, 0x2000
	global_load_lds_dwordx4 v[10:11], off
	v_lshl_add_u64 v[10:11], s[42:43], 0, v[148:149]
	s_mov_b32 m0, s18
	s_nop 0
	global_load_lds_dwordx4 v[10:11], off
	s_waitcnt vmcnt(6)
	s_barrier
	s_setprio 1
	v_mov_b64_e32 v[68:69], v[4:5]
	v_mov_b64_e32 v[56:57], v[4:5]
	v_mov_b64_e32 v[44:45], v[4:5]
	v_mov_b64_e32 v[36:37], v[4:5]
	v_mov_b64_e32 v[28:29], v[4:5]
	v_mov_b64_e32 v[20:21], v[4:5]
	v_mov_b64_e32 v[12:13], v[4:5]
	v_mov_b64_e32 v[66:67], v[2:3]
	v_mov_b64_e32 v[54:55], v[2:3]
	v_mov_b64_e32 v[42:43], v[2:3]
	v_mov_b64_e32 v[34:35], v[2:3]
	v_mov_b64_e32 v[26:27], v[2:3]
	v_mov_b64_e32 v[18:19], v[2:3]
	v_mov_b64_e32 v[10:11], v[2:3]
	v_mfma_scale_f32_16x16x128_f8f6f4 v[66:69], v[172:179], v[188:195], v[66:69], v210, v210 op_sel_hi:[0,0,0]
	v_mfma_scale_f32_16x16x128_f8f6f4 v[54:57], v[180:187], v[188:195], v[54:57], v210, v210 op_sel_hi:[0,0,0]
	v_mfma_scale_f32_16x16x128_f8f6f4 v[42:45], v[172:179], v[196:203], v[42:45], v210, v210 op_sel_hi:[0,0,0]
	v_mfma_scale_f32_16x16x128_f8f6f4 v[34:37], v[180:187], v[196:203], v[34:37], v210, v210 op_sel_hi:[0,0,0]
	v_mfma_scale_f32_16x16x128_f8f6f4 v[26:29], v[172:179], v[218:225], v[26:29], v210, v210 op_sel_hi:[0,0,0]
	v_mfma_scale_f32_16x16x128_f8f6f4 v[18:21], v[180:187], v[218:225], v[18:21], v210, v210 op_sel_hi:[0,0,0]
	v_mfma_scale_f32_16x16x128_f8f6f4 v[10:13], v[172:179], v[226:233], v[10:13], v210, v210 op_sel_hi:[0,0,0]
	v_mfma_scale_f32_16x16x128_f8f6f4 v[2:5], v[180:187], v[226:233], v[2:5], v210, v210 op_sel_hi:[0,0,0]
	s_setprio 0
	s_add_i32 s42, 0, 0x18000
	v_add_u32_e32 v144, s42, v215
	s_barrier
	ds_read_b128 v[164:167], v144
	ds_read_b128 v[168:171], v144 offset:1024
	ds_read_b128 v[172:175], v144 offset:2048
	ds_read_b128 v[176:179], v144 offset:3072
	s_mov_b32 m0, s9
	v_lshl_add_u64 v[160:161], v[130:131], 0, s[84:85]
	ds_read_b128 v[180:183], v217 offset:32768
	ds_read_b128 v[184:187], v217 offset:33792
	ds_read_b128 v[188:191], v217 offset:34816
	ds_read_b128 v[192:195], v217 offset:35840
	ds_read_b128 v[196:199], v217 offset:36864
	ds_read_b128 v[200:203], v217 offset:37888
	ds_read_b128 v[218:221], v217 offset:38912
	ds_read_b128 v[222:225], v217 offset:39936
	global_load_lds_dwordx4 v[160:161], off
	v_lshl_add_u64 v[160:161], v[132:133], 0, s[84:85]
	s_mov_b32 m0, s82
	s_nop 0
	global_load_lds_dwordx4 v[160:161], off
	s_waitcnt lgkmcnt(8)
	s_barrier
	s_waitcnt lgkmcnt(0)
	s_setprio 1
	s_waitcnt lgkmcnt(0)
	v_mfma_scale_f32_16x16x128_f8f6f4 v[118:121], v[164:171], v[180:187], v[118:121], v210, v210 op_sel_hi:[0,0,0]
	v_mfma_scale_f32_16x16x128_f8f6f4 v[114:117], v[172:179], v[180:187], v[114:117], v210, v210 op_sel_hi:[0,0,0]
	v_mfma_scale_f32_16x16x128_f8f6f4 v[102:105], v[164:171], v[188:195], v[102:105], v210, v210 op_sel_hi:[0,0,0]
	v_mfma_scale_f32_16x16x128_f8f6f4 v[98:101], v[172:179], v[188:195], v[98:101], v210, v210 op_sel_hi:[0,0,0]
	v_mfma_scale_f32_16x16x128_f8f6f4 v[86:89], v[164:171], v[196:203], v[86:89], v210, v210 op_sel_hi:[0,0,0]
	v_mfma_scale_f32_16x16x128_f8f6f4 v[82:85], v[172:179], v[196:203], v[82:85], v210, v210 op_sel_hi:[0,0,0]
	v_mfma_scale_f32_16x16x128_f8f6f4 v[58:61], v[164:171], v[218:225], v[58:61], v210, v210 op_sel_hi:[0,0,0]
	v_mfma_scale_f32_16x16x128_f8f6f4 v[50:53], v[172:179], v[218:225], v[50:53], v210, v210 op_sel_hi:[0,0,0]
	s_setprio 0
	s_barrier
	s_add_i32 s43, 0, 0x1c000
	s_add_i32 s42, s42, s87
	v_add_u32_e32 v145, s43, v215
	v_lshl_add_u64 v[134:135], v[134:135], 0, s[58:59]
	s_mov_b32 m0, s42
	s_add_i32 s25, s42, 0x2000
	ds_read_b128 v[226:229], v145
	ds_read_b128 v[230:233], v145 offset:1024
	ds_read_b128 v[234:237], v145 offset:2048
	ds_read_b128 v[238:241], v145 offset:3072
	global_load_lds_dwordx4 v[134:135], off
	v_lshl_add_u64 v[134:135], v[136:137], 0, s[58:59]
	s_mov_b32 m0, s25
	s_nop 0
	global_load_lds_dwordx4 v[134:135], off
	s_barrier
	s_waitcnt lgkmcnt(0)
	s_setprio 1
	s_waitcnt lgkmcnt(0)
	v_mfma_scale_f32_16x16x128_f8f6f4 v[126:129], v[226:233], v[180:187], v[126:129], v210, v210 op_sel_hi:[0,0,0]
	v_mfma_scale_f32_16x16x128_f8f6f4 v[122:125], v[234:241], v[180:187], v[122:125], v210, v210 op_sel_hi:[0,0,0]
	v_mfma_scale_f32_16x16x128_f8f6f4 v[110:113], v[226:233], v[188:195], v[110:113], v210, v210 op_sel_hi:[0,0,0]
	v_mfma_scale_f32_16x16x128_f8f6f4 v[106:109], v[234:241], v[188:195], v[106:109], v210, v210 op_sel_hi:[0,0,0]
	v_mfma_scale_f32_16x16x128_f8f6f4 v[94:97], v[226:233], v[196:203], v[94:97], v210, v210 op_sel_hi:[0,0,0]
	v_mfma_scale_f32_16x16x128_f8f6f4 v[90:93], v[234:241], v[196:203], v[90:93], v210, v210 op_sel_hi:[0,0,0]
	v_mfma_scale_f32_16x16x128_f8f6f4 v[78:81], v[226:233], v[218:225], v[78:81], v210, v210 op_sel_hi:[0,0,0]
	v_mfma_scale_f32_16x16x128_f8f6f4 v[74:77], v[234:241], v[218:225], v[74:77], v210, v210 op_sel_hi:[0,0,0]
	s_setprio 0
	s_mov_b32 m0, s83
	v_lshl_add_u64 v[134:135], v[138:139], 0, s[58:59]
	s_barrier
	ds_read_b128 v[180:183], v217 offset:49152
	ds_read_b128 v[184:187], v217 offset:50176
	ds_read_b128 v[188:191], v217 offset:51200
	ds_read_b128 v[192:195], v217 offset:52224
	ds_read_b128 v[196:199], v217 offset:53248
	ds_read_b128 v[200:203], v217 offset:54272
	ds_read_b128 v[218:221], v217 offset:55296
	ds_read_b128 v[222:225], v217 offset:56320
	global_load_lds_dwordx4 v[134:135], off
	v_lshl_add_u64 v[134:135], v[140:141], 0, s[58:59]
	s_mov_b32 m0, s5
	s_nop 0
	global_load_lds_dwordx4 v[134:135], off
	s_barrier
	s_waitcnt lgkmcnt(0)
	s_setprio 1
	s_waitcnt lgkmcnt(0)
	v_mfma_scale_f32_16x16x128_f8f6f4 v[70:73], v[164:171], v[180:187], v[70:73], v210, v210 op_sel_hi:[0,0,0]
	v_mfma_scale_f32_16x16x128_f8f6f4 v[62:65], v[172:179], v[180:187], v[62:65], v210, v210 op_sel_hi:[0,0,0]
	v_mfma_scale_f32_16x16x128_f8f6f4 v[46:49], v[164:171], v[188:195], v[46:49], v210, v210 op_sel_hi:[0,0,0]
	v_mfma_scale_f32_16x16x128_f8f6f4 v[38:41], v[172:179], v[188:195], v[38:41], v210, v210 op_sel_hi:[0,0,0]
	v_mfma_scale_f32_16x16x128_f8f6f4 v[30:33], v[164:171], v[196:203], v[30:33], v210, v210 op_sel_hi:[0,0,0]
	v_mfma_scale_f32_16x16x128_f8f6f4 v[22:25], v[172:179], v[196:203], v[22:25], v210, v210 op_sel_hi:[0,0,0]
	v_mfma_scale_f32_16x16x128_f8f6f4 v[14:17], v[164:171], v[218:225], v[14:17], v210, v210 op_sel_hi:[0,0,0]
	v_mfma_scale_f32_16x16x128_f8f6f4 v[6:9], v[172:179], v[218:225], v[6:9], v210, v210 op_sel_hi:[0,0,0]
	s_setprio 0
	s_barrier
	s_add_u32 s90, s20, 0x10180
	s_addc_u32 s91, s21, 0
	s_add_i32 s21, s43, s87
	v_lshl_add_u64 v[134:135], s[90:91], 0, v[146:147]
	s_mov_b32 m0, s21
	s_add_i32 s20, s21, 0x2000
	global_load_lds_dwordx4 v[134:135], off
	v_lshl_add_u64 v[134:135], s[90:91], 0, v[148:149]
	s_mov_b32 m0, s20
	s_nop 0
	global_load_lds_dwordx4 v[134:135], off
	s_waitcnt vmcnt(6)
	s_barrier
	s_setprio 1
	v_mfma_scale_f32_16x16x128_f8f6f4 v[66:69], v[226:233], v[180:187], v[66:69], v210, v210 op_sel_hi:[0,0,0]
	v_mfma_scale_f32_16x16x128_f8f6f4 v[54:57], v[234:241], v[180:187], v[54:57], v210, v210 op_sel_hi:[0,0,0]
	v_mfma_scale_f32_16x16x128_f8f6f4 v[42:45], v[226:233], v[188:195], v[42:45], v210, v210 op_sel_hi:[0,0,0]
	v_mfma_scale_f32_16x16x128_f8f6f4 v[34:37], v[234:241], v[188:195], v[34:37], v210, v210 op_sel_hi:[0,0,0]
	v_mfma_scale_f32_16x16x128_f8f6f4 v[26:29], v[226:233], v[196:203], v[26:29], v210, v210 op_sel_hi:[0,0,0]
	v_mfma_scale_f32_16x16x128_f8f6f4 v[18:21], v[234:241], v[196:203], v[18:21], v210, v210 op_sel_hi:[0,0,0]
	v_mfma_scale_f32_16x16x128_f8f6f4 v[10:13], v[226:233], v[218:225], v[10:13], v210, v210 op_sel_hi:[0,0,0]
	v_mfma_scale_f32_16x16x128_f8f6f4 v[2:5], v[234:241], v[218:225], v[2:5], v210, v210 op_sel_hi:[0,0,0]
	s_setprio 0
	s_barrier
	ds_read_b128 v[134:137], v142
	ds_read_b128 v[138:141], v142 offset:1024
	ds_read_b128 v[164:167], v142 offset:2048
	ds_read_b128 v[168:171], v142 offset:3072
	s_mov_b32 m0, s61
	v_lshl_add_u64 v[130:131], v[130:131], 0, s[58:59]
	ds_read_b128 v[172:175], v217
	ds_read_b128 v[176:179], v217 offset:1024
	ds_read_b128 v[180:183], v217 offset:2048
	ds_read_b128 v[184:187], v217 offset:3072
	ds_read_b128 v[188:191], v217 offset:4096
	ds_read_b128 v[192:195], v217 offset:5120
	ds_read_b128 v[196:199], v217 offset:6144
	ds_read_b128 v[200:203], v217 offset:7168
	global_load_lds_dwordx4 v[130:131], off
	v_lshl_add_u64 v[130:131], v[132:133], 0, s[58:59]
	s_mov_b32 m0, s13
	s_nop 0
	global_load_lds_dwordx4 v[130:131], off
	s_waitcnt lgkmcnt(8)
	s_barrier
	s_waitcnt lgkmcnt(0)
	s_setprio 1
	s_waitcnt lgkmcnt(0)
	v_mfma_scale_f32_16x16x128_f8f6f4 v[118:121], v[134:141], v[172:179], v[118:121], v210, v210 op_sel_hi:[0,0,0]
	v_mfma_scale_f32_16x16x128_f8f6f4 v[114:117], v[164:171], v[172:179], v[114:117], v210, v210 op_sel_hi:[0,0,0]
	v_mfma_scale_f32_16x16x128_f8f6f4 v[102:105], v[134:141], v[180:187], v[102:105], v210, v210 op_sel_hi:[0,0,0]
	v_mfma_scale_f32_16x16x128_f8f6f4 v[98:101], v[164:171], v[180:187], v[98:101], v210, v210 op_sel_hi:[0,0,0]
	v_mfma_scale_f32_16x16x128_f8f6f4 v[86:89], v[134:141], v[188:195], v[86:89], v210, v210 op_sel_hi:[0,0,0]
	v_mfma_scale_f32_16x16x128_f8f6f4 v[82:85], v[164:171], v[188:195], v[82:85], v210, v210 op_sel_hi:[0,0,0]
	v_mfma_scale_f32_16x16x128_f8f6f4 v[58:61], v[134:141], v[196:203], v[58:61], v210, v210 op_sel_hi:[0,0,0]
	v_mfma_scale_f32_16x16x128_f8f6f4 v[50:53], v[164:171], v[196:203], v[50:53], v210, v210 op_sel_hi:[0,0,0]
	s_setprio 0
	s_barrier
	s_mov_b32 m0, s41
	v_lshl_add_u64 v[160:161], s[26:27], 0, v[146:147]
	ds_read_b128 v[218:221], v143
	ds_read_b128 v[222:225], v143 offset:1024
	ds_read_b128 v[226:229], v143 offset:2048
	ds_read_b128 v[230:233], v143 offset:3072
	global_load_lds_dwordx4 v[160:161], off
	v_lshl_add_u64 v[204:205], s[26:27], 0, v[148:149]
	s_mov_b32 m0, s23
	s_nop 0
	global_load_lds_dwordx4 v[204:205], off
	s_barrier
	s_waitcnt lgkmcnt(0)
	s_setprio 1
	s_waitcnt lgkmcnt(0)
	v_mfma_scale_f32_16x16x128_f8f6f4 v[126:129], v[218:225], v[172:179], v[126:129], v210, v210 op_sel_hi:[0,0,0]
	v_mfma_scale_f32_16x16x128_f8f6f4 v[122:125], v[226:233], v[172:179], v[122:125], v210, v210 op_sel_hi:[0,0,0]
	v_mfma_scale_f32_16x16x128_f8f6f4 v[110:113], v[218:225], v[180:187], v[110:113], v210, v210 op_sel_hi:[0,0,0]
	v_mfma_scale_f32_16x16x128_f8f6f4 v[106:109], v[226:233], v[180:187], v[106:109], v210, v210 op_sel_hi:[0,0,0]
	v_mfma_scale_f32_16x16x128_f8f6f4 v[94:97], v[218:225], v[188:195], v[94:97], v210, v210 op_sel_hi:[0,0,0]
	v_mfma_scale_f32_16x16x128_f8f6f4 v[90:93], v[226:233], v[188:195], v[90:93], v210, v210 op_sel_hi:[0,0,0]
	v_mfma_scale_f32_16x16x128_f8f6f4 v[78:81], v[218:225], v[196:203], v[78:81], v210, v210 op_sel_hi:[0,0,0]
	v_mfma_scale_f32_16x16x128_f8f6f4 v[74:77], v[226:233], v[196:203], v[74:77], v210, v210 op_sel_hi:[0,0,0]
	s_setprio 0
	s_mov_b32 m0, s15
	v_lshl_add_u64 v[206:207], s[28:29], 0, v[150:151]
	s_barrier
	ds_read_b128 v[172:175], v217 offset:16384
	ds_read_b128 v[176:179], v217 offset:17408
	ds_read_b128 v[180:183], v217 offset:18432
	ds_read_b128 v[184:187], v217 offset:19456
	ds_read_b128 v[188:191], v217 offset:20480
	ds_read_b128 v[192:195], v217 offset:21504
	ds_read_b128 v[196:199], v217 offset:22528
	ds_read_b128 v[200:203], v217 offset:23552
	global_load_lds_dwordx4 v[206:207], off
	v_lshl_add_u64 v[208:209], s[28:29], 0, v[152:153]
	s_mov_b32 m0, s8
	s_nop 0
	global_load_lds_dwordx4 v[208:209], off
	s_barrier
	s_waitcnt lgkmcnt(0)
	s_setprio 1
	s_waitcnt lgkmcnt(0)
	v_mfma_scale_f32_16x16x128_f8f6f4 v[70:73], v[134:141], v[172:179], v[70:73], v210, v210 op_sel_hi:[0,0,0]
	v_mfma_scale_f32_16x16x128_f8f6f4 v[62:65], v[164:171], v[172:179], v[62:65], v210, v210 op_sel_hi:[0,0,0]
	v_mfma_scale_f32_16x16x128_f8f6f4 v[46:49], v[134:141], v[180:187], v[46:49], v210, v210 op_sel_hi:[0,0,0]
	v_mfma_scale_f32_16x16x128_f8f6f4 v[38:41], v[164:171], v[180:187], v[38:41], v210, v210 op_sel_hi:[0,0,0]
	v_mfma_scale_f32_16x16x128_f8f6f4 v[30:33], v[134:141], v[188:195], v[30:33], v210, v210 op_sel_hi:[0,0,0]
	v_mfma_scale_f32_16x16x128_f8f6f4 v[22:25], v[164:171], v[188:195], v[22:25], v210, v210 op_sel_hi:[0,0,0]
	v_mfma_scale_f32_16x16x128_f8f6f4 v[14:17], v[134:141], v[196:203], v[14:17], v210, v210 op_sel_hi:[0,0,0]
	v_mfma_scale_f32_16x16x128_f8f6f4 v[6:9], v[164:171], v[196:203], v[6:9], v210, v210 op_sel_hi:[0,0,0]
	s_setprio 0
	s_barrier
	s_add_u32 s90, s26, 0x10000
	s_addc_u32 s91, s27, 0
	s_mov_b32 m0, s19
	v_lshl_add_u64 v[130:131], s[90:91], 0, v[146:147]
	global_load_lds_dwordx4 v[130:131], off
	v_lshl_add_u64 v[130:131], s[90:91], 0, v[148:149]
	s_mov_b32 m0, s18
	s_nop 0
	global_load_lds_dwordx4 v[130:131], off
	s_waitcnt vmcnt(6)
	s_barrier
	s_setprio 1
	v_mfma_scale_f32_16x16x128_f8f6f4 v[66:69], v[218:225], v[172:179], v[66:69], v210, v210 op_sel_hi:[0,0,0]
	v_mfma_scale_f32_16x16x128_f8f6f4 v[54:57], v[226:233], v[172:179], v[54:57], v210, v210 op_sel_hi:[0,0,0]
	v_mfma_scale_f32_16x16x128_f8f6f4 v[42:45], v[218:225], v[180:187], v[42:45], v210, v210 op_sel_hi:[0,0,0]
	v_mfma_scale_f32_16x16x128_f8f6f4 v[34:37], v[226:233], v[180:187], v[34:37], v210, v210 op_sel_hi:[0,0,0]
	v_mfma_scale_f32_16x16x128_f8f6f4 v[26:29], v[218:225], v[188:195], v[26:29], v210, v210 op_sel_hi:[0,0,0]
	v_mfma_scale_f32_16x16x128_f8f6f4 v[18:21], v[226:233], v[188:195], v[18:21], v210, v210 op_sel_hi:[0,0,0]
	v_mfma_scale_f32_16x16x128_f8f6f4 v[10:13], v[218:225], v[196:203], v[10:13], v210, v210 op_sel_hi:[0,0,0]
	v_mfma_scale_f32_16x16x128_f8f6f4 v[2:5], v[226:233], v[196:203], v[2:5], v210, v210 op_sel_hi:[0,0,0]
	s_setprio 0
	s_barrier
	ds_read_b128 v[130:133], v144
	ds_read_b128 v[134:137], v144 offset:1024
	ds_read_b128 v[164:167], v144 offset:2048
	ds_read_b128 v[168:171], v144 offset:3072
	s_mov_b32 m0, s9
	v_lshl_add_u64 v[138:139], s[28:29], 0, v[154:155]
	ds_read_b128 v[172:175], v217 offset:32768
	ds_read_b128 v[176:179], v217 offset:33792
	ds_read_b128 v[180:183], v217 offset:34816
	ds_read_b128 v[184:187], v217 offset:35840
	ds_read_b128 v[188:191], v217 offset:36864
	ds_read_b128 v[192:195], v217 offset:37888
	ds_read_b128 v[196:199], v217 offset:38912
	ds_read_b128 v[200:203], v217 offset:39936
	global_load_lds_dwordx4 v[138:139], off
	v_lshl_add_u64 v[138:139], s[28:29], 0, v[156:157]
	s_mov_b32 m0, s82
	s_nop 0
	global_load_lds_dwordx4 v[138:139], off
	s_waitcnt lgkmcnt(8)
	s_barrier
	s_waitcnt lgkmcnt(0)
	s_setprio 1
	s_waitcnt lgkmcnt(0)
	v_mfma_scale_f32_16x16x128_f8f6f4 v[118:121], v[130:137], v[172:179], v[118:121], v210, v210 op_sel_hi:[0,0,0]
	v_mfma_scale_f32_16x16x128_f8f6f4 v[114:117], v[164:171], v[172:179], v[114:117], v210, v210 op_sel_hi:[0,0,0]
	v_mfma_scale_f32_16x16x128_f8f6f4 v[102:105], v[130:137], v[180:187], v[102:105], v210, v210 op_sel_hi:[0,0,0]
	v_mfma_scale_f32_16x16x128_f8f6f4 v[98:101], v[164:171], v[180:187], v[98:101], v210, v210 op_sel_hi:[0,0,0]
	v_mfma_scale_f32_16x16x128_f8f6f4 v[86:89], v[130:137], v[188:195], v[86:89], v210, v210 op_sel_hi:[0,0,0]
	v_mfma_scale_f32_16x16x128_f8f6f4 v[82:85], v[164:171], v[188:195], v[82:85], v210, v210 op_sel_hi:[0,0,0]
	v_mfma_scale_f32_16x16x128_f8f6f4 v[58:61], v[130:137], v[196:203], v[58:61], v210, v210 op_sel_hi:[0,0,0]
	v_mfma_scale_f32_16x16x128_f8f6f4 v[50:53], v[164:171], v[196:203], v[50:53], v210, v210 op_sel_hi:[0,0,0]
	s_setprio 0
	s_barrier
	s_mov_b32 m0, s42
	v_lshl_add_u64 v[160:161], v[160:161], 0, s[44:45]
	ds_read_b128 v[218:221], v145
	ds_read_b128 v[222:225], v145 offset:1024
	ds_read_b128 v[138:141], v145 offset:2048
	ds_read_b128 v[142:145], v145 offset:3072
	global_load_lds_dwordx4 v[160:161], off
	v_lshl_add_u64 v[160:161], v[204:205], 0, s[44:45]
	s_mov_b32 m0, s25
	s_nop 0
	global_load_lds_dwordx4 v[160:161], off
	s_barrier
	s_waitcnt lgkmcnt(0)
	s_setprio 1
	s_waitcnt lgkmcnt(0)
	v_mfma_scale_f32_16x16x128_f8f6f4 v[126:129], v[218:225], v[172:179], v[126:129], v210, v210 op_sel_hi:[0,0,0]
	v_mfma_scale_f32_16x16x128_f8f6f4 v[122:125], v[138:145], v[172:179], v[122:125], v210, v210 op_sel_hi:[0,0,0]
	v_mfma_scale_f32_16x16x128_f8f6f4 v[110:113], v[218:225], v[180:187], v[110:113], v210, v210 op_sel_hi:[0,0,0]
	v_mfma_scale_f32_16x16x128_f8f6f4 v[106:109], v[138:145], v[180:187], v[106:109], v210, v210 op_sel_hi:[0,0,0]
	v_mfma_scale_f32_16x16x128_f8f6f4 v[94:97], v[218:225], v[188:195], v[94:97], v210, v210 op_sel_hi:[0,0,0]
	v_mfma_scale_f32_16x16x128_f8f6f4 v[90:93], v[138:145], v[188:195], v[90:93], v210, v210 op_sel_hi:[0,0,0]
	v_mfma_scale_f32_16x16x128_f8f6f4 v[78:81], v[218:225], v[196:203], v[78:81], v210, v210 op_sel_hi:[0,0,0]
	v_mfma_scale_f32_16x16x128_f8f6f4 v[74:77], v[138:145], v[196:203], v[74:77], v210, v210 op_sel_hi:[0,0,0]
	s_setprio 0
	s_mov_b32 m0, s83
	v_lshl_add_u64 v[160:161], v[206:207], 0, s[44:45]
	s_barrier
	ds_read_b128 v[172:175], v217 offset:49152
	ds_read_b128 v[176:179], v217 offset:50176
	ds_read_b128 v[180:183], v217 offset:51200
	ds_read_b128 v[184:187], v217 offset:52224
	ds_read_b128 v[188:191], v217 offset:53248
	ds_read_b128 v[192:195], v217 offset:54272
	ds_read_b128 v[196:199], v217 offset:55296
	ds_read_b128 v[200:203], v217 offset:56320
	global_load_lds_dwordx4 v[160:161], off
	v_lshl_add_u64 v[160:161], v[208:209], 0, s[44:45]
	s_mov_b32 m0, s5
	s_nop 0
	global_load_lds_dwordx4 v[160:161], off
	s_barrier
	s_waitcnt lgkmcnt(0)
	s_setprio 1
	s_waitcnt lgkmcnt(0)
	v_mfma_scale_f32_16x16x128_f8f6f4 v[70:73], v[130:137], v[172:179], v[70:73], v210, v210 op_sel_hi:[0,0,0]
	v_mfma_scale_f32_16x16x128_f8f6f4 v[62:65], v[164:171], v[172:179], v[62:65], v210, v210 op_sel_hi:[0,0,0]
	v_mfma_scale_f32_16x16x128_f8f6f4 v[46:49], v[130:137], v[180:187], v[46:49], v210, v210 op_sel_hi:[0,0,0]
	v_mfma_scale_f32_16x16x128_f8f6f4 v[38:41], v[164:171], v[180:187], v[38:41], v210, v210 op_sel_hi:[0,0,0]
	v_mfma_scale_f32_16x16x128_f8f6f4 v[30:33], v[130:137], v[188:195], v[30:33], v210, v210 op_sel_hi:[0,0,0]
	v_mfma_scale_f32_16x16x128_f8f6f4 v[22:25], v[164:171], v[188:195], v[22:25], v210, v210 op_sel_hi:[0,0,0]
	v_mfma_scale_f32_16x16x128_f8f6f4 v[14:17], v[130:137], v[196:203], v[14:17], v210, v210 op_sel_hi:[0,0,0]
	v_mfma_scale_f32_16x16x128_f8f6f4 v[6:9], v[164:171], v[196:203], v[6:9], v210, v210 op_sel_hi:[0,0,0]
	s_setprio 0
	s_barrier
	s_add_u32 s18, s26, 0x10080
	s_addc_u32 s19, s27, 0
	s_mov_b32 m0, s21
	v_lshl_add_u64 v[130:131], s[18:19], 0, v[146:147]
	global_load_lds_dwordx4 v[130:131], off
	v_lshl_add_u64 v[130:131], s[18:19], 0, v[148:149]
	s_mov_b32 m0, s20
	s_nop 0
	global_load_lds_dwordx4 v[130:131], off
	s_waitcnt vmcnt(6)
	s_barrier
	s_setprio 1
	v_mfma_scale_f32_16x16x128_f8f6f4 v[66:69], v[218:225], v[172:179], v[66:69], v210, v210 op_sel_hi:[0,0,0]
	v_mfma_scale_f32_16x16x128_f8f6f4 v[54:57], v[138:145], v[172:179], v[54:57], v210, v210 op_sel_hi:[0,0,0]
	v_mfma_scale_f32_16x16x128_f8f6f4 v[42:45], v[218:225], v[180:187], v[42:45], v210, v210 op_sel_hi:[0,0,0]
	v_mfma_scale_f32_16x16x128_f8f6f4 v[34:37], v[138:145], v[180:187], v[34:37], v210, v210 op_sel_hi:[0,0,0]
	v_mfma_scale_f32_16x16x128_f8f6f4 v[26:29], v[218:225], v[188:195], v[26:29], v210, v210 op_sel_hi:[0,0,0]
	v_mfma_scale_f32_16x16x128_f8f6f4 v[18:21], v[138:145], v[188:195], v[18:21], v210, v210 op_sel_hi:[0,0,0]
	v_mfma_scale_f32_16x16x128_f8f6f4 v[10:13], v[218:225], v[196:203], v[10:13], v210, v210 op_sel_hi:[0,0,0]
	v_mfma_scale_f32_16x16x128_f8f6f4 v[2:5], v[138:145], v[196:203], v[2:5], v210, v210 op_sel_hi:[0,0,0]
	s_setprio 0
	v_lshl_add_u32 v130, s14, 8, v214
	v_ashrrev_i32_e32 v131, 31, v130
	v_lshl_add_u64 v[130:131], v[130:131], 3, s[0:1]
	s_barrier
	s_nop 15
	s_nop 15
	global_load_dwordx2 v[176:177], v[130:131], off
	global_load_dwordx2 v[174:175], v[130:131], off offset:128
	global_load_dwordx2 v[172:173], v[130:131], off offset:256
	global_load_dwordx2 v[170:171], v[130:131], off offset:384
	global_load_dwordx2 v[168:169], v[130:131], off offset:1024
	global_load_dwordx2 v[166:167], v[130:131], off offset:1152
	global_load_dwordx2 v[164:165], v[130:131], off offset:1280
	global_load_dwordx2 v[160:161], v[130:131], off offset:1408
	s_cmp_lt_i32 s12, 64
	s_cbranch_scc1 .LBB0_3627
	s_waitcnt vmcnt(0)
	v_ashrrev_i32_e32 v130, 13, v177
	v_mul_i32_i24_e32 v130, 0x3000, v130
	v_lshl_or_b32 v186, s51, 8, v216
	v_ashrrev_i32_e32 v131, 31, v130
	v_ashrrev_i32_e32 v187, 31, v186
	v_lshl_add_u64 v[130:131], v[130:131], 2, s[46:47]
	s_mov_b64 s[12:13], 0xf000
	v_lshlrev_b64 v[178:179], 1, v[186:187]
	v_ashrrev_i32_e32 v139, 31, v177
	v_mov_b32_e32 v138, v177
	v_lshl_add_u64 v[188:189], v[130:131], 0, s[12:13]
	v_lshl_add_u64 v[180:181], s[6:7], 0, v[178:179]
	v_lshlrev_b64 v[190:191], 12, v[138:139]
	v_lshl_add_u64 v[182:183], v[186:187], 2, v[188:189]
	v_lshl_add_u64 v[138:139], v[180:181], 0, v[190:191]
	global_load_dwordx4 v[130:133], v[182:183], off offset:16
	global_load_dwordx4 v[134:137], v[182:183], off
	global_load_dwordx4 v[196:199], v[138:139], off
	v_ashrrev_i32_e32 v139, 31, v175
	v_mov_b32_e32 v138, v175
	v_lshlrev_b64 v[184:185], 12, v[138:139]
	v_lshl_add_u64 v[138:139], v[180:181], 0, v[184:185]
	global_load_dwordx4 v[206:209], v[138:139], off
	v_ashrrev_i32_e32 v139, 31, v173
	v_mov_b32_e32 v138, v173
	v_lshlrev_b64 v[192:193], 12, v[138:139]
	v_lshl_add_u64 v[138:139], v[180:181], 0, v[192:193]
	global_load_dwordx4 v[142:145], v[138:139], off
	v_ashrrev_i32_e32 v139, 31, v171
	v_mov_b32_e32 v138, v171
	v_lshlrev_b64 v[194:195], 12, v[138:139]
	v_lshl_add_u64 v[138:139], v[180:181], 0, v[194:195]
	global_load_dwordx4 v[138:141], v[138:139], off
	v_mov_b32_e32 v200, v118
	v_mov_b32_e32 v218, v114
	v_mov_b32_e32 v202, v119
	v_mov_b32_e32 v220, v115
	v_mov_b32_e32 v204, v120
	v_mov_b32_e32 v222, v116
	s_mov_b64 vcc, 0
	s_waitcnt vmcnt(0)
	v_lshlrev_b32_e32 v201, 16, v196
	v_and_b32_e32 v203, 0xffff0000, v196
	v_lshlrev_b32_e32 v205, 16, v197
	v_and_b32_e32 v197, 0xffff0000, v197
	v_lshlrev_b32_e32 v219, 16, v198
	v_and_b32_e32 v221, 0xffff0000, v198
	v_lshlrev_b32_e32 v223, 16, v199
	v_and_b32_e32 v199, 0xffff0000, v199
	v_pk_mul_f32 v[200:201], v[200:201], s[56:57]
	v_mov_b32_e32 v196, v121
	v_mov_b32_e32 v198, v117
	v_fmac_f32_e32 v201, v200, v134
	v_pk_mul_f32 v[218:219], v[218:219], s[56:57]
	v_pk_mul_f32 v[202:203], v[202:203], s[56:57]
	v_pk_mul_f32 v[220:221], v[220:221], s[56:57]
	v_pk_mul_f32 v[204:205], v[204:205], s[56:57]
	v_pk_mul_f32 v[222:223], v[222:223], s[56:57]
	v_pk_mul_f32 v[224:225], v[196:197], s[56:57]
	v_pk_mul_f32 v[226:227], v[198:199], s[56:57]
	v_lshl_add_u64 v[196:197], s[62:63], 0, v[190:191]
	v_fmac_f32_e32 v219, v218, v130
	v_fmac_f32_e32 v203, v202, v135
	v_fmac_f32_e32 v221, v220, v131
	v_fmac_f32_e32 v205, v204, v136
	v_fmac_f32_e32 v223, v222, v132
	v_fmac_f32_e32 v225, v224, v137
	v_fmac_f32_e32 v227, v226, v133
	v_lshl_add_u64 v[196:197], v[196:197], 0, v[178:179]
	v_cvt_pk_bf16_f32 v198, v201, v203
	v_cvt_pk_bf16_f32 v199, v205, v225
	v_cvt_pk_bf16_f32 v200, v219, v221
	v_cvt_pk_bf16_f32 v201, v223, v227
	global_store_dwordx4 v[196:197], v[198:201], off
	v_lshlrev_b32_e32 v219, 16, v206
	v_and_b32_e32 v221, 0xffff0000, v206
	v_and_b32_e32 v201, 0xffff0000, v207
	v_mov_b32_e32 v200, v105
	v_lshlrev_b32_e32 v205, 16, v207
	v_lshlrev_b32_e32 v223, 16, v208
	v_lshlrev_b32_e32 v203, 16, v209
	v_and_b32_e32 v199, 0xffff0000, v209
	v_mov_b32_e32 v218, v102
	v_mov_b32_e32 v222, v98
	v_mov_b32_e32 v220, v103
	v_mov_b32_e32 v204, v104
	v_mov_b32_e32 v202, v100
	v_pk_mul_f32 v[200:201], v[200:201], s[56:57]
	v_mov_b32_e32 v198, v101
	v_and_b32_e32 v207, 0xffff0000, v208
	v_pk_mul_f32 v[208:209], v[218:219], s[56:57]
	v_pk_mul_f32 v[218:219], v[222:223], s[56:57]
	v_pk_mul_f32 v[220:221], v[220:221], s[56:57]
	v_mov_b32_e32 v206, v99
	v_pk_mul_f32 v[204:205], v[204:205], s[56:57]
	v_pk_mul_f32 v[202:203], v[202:203], s[56:57]
	v_fmac_f32_e32 v201, v200, v137
	v_pk_mul_f32 v[222:223], v[198:199], s[56:57]
	v_lshl_add_u64 v[198:199], s[62:63], 0, v[184:185]
	v_fmac_f32_e32 v209, v208, v134
	v_fmac_f32_e32 v221, v220, v135
	v_pk_mul_f32 v[206:207], v[206:207], s[56:57]
	v_fmac_f32_e32 v205, v204, v136
	v_fmac_f32_e32 v203, v202, v132
	v_lshl_add_u64 v[198:199], v[198:199], 0, v[178:179]
	v_cvt_pk_bf16_f32 v200, v209, v221
	v_cvt_pk_bf16_f32 v201, v205, v201
	v_fmac_f32_e32 v219, v218, v130
	v_fmac_f32_e32 v207, v206, v131
	v_fmac_f32_e32 v223, v222, v133
	v_cvt_pk_bf16_f32 v202, v219, v207
	v_cvt_pk_bf16_f32 v203, v203, v223
	global_store_dwordx4 v[198:199], v[200:203], off
	v_lshlrev_b32_e32 v205, 16, v143
	v_and_b32_e32 v143, 0xffff0000, v143
	v_lshlrev_b32_e32 v201, 16, v142
	v_mov_b32_e32 v200, v86
	v_and_b32_e32 v203, 0xffff0000, v142
	v_lshlrev_b32_e32 v207, 16, v144
	v_and_b32_e32 v209, 0xffff0000, v144
	v_lshlrev_b32_e32 v219, 16, v145
	v_and_b32_e32 v145, 0xffff0000, v145
	v_pk_mul_f32 v[200:201], v[200:201], s[56:57]
	v_mov_b32_e32 v202, v87
	v_mov_b32_e32 v204, v88
	v_mov_b32_e32 v142, v89
	v_mov_b32_e32 v144, v85
	v_fmac_f32_e32 v201, v200, v134
	v_mov_b32_e32 v206, v82
	v_pk_mul_f32 v[202:203], v[202:203], s[56:57]
	v_mov_b32_e32 v208, v83
	v_pk_mul_f32 v[204:205], v[204:205], s[56:57]
	v_mov_b32_e32 v218, v84
	v_pk_mul_f32 v[220:221], v[142:143], s[56:57]
	v_pk_mul_f32 v[144:145], v[144:145], s[56:57]
	v_lshl_add_u64 v[142:143], s[62:63], 0, v[192:193]
	v_pk_mul_f32 v[206:207], v[206:207], s[56:57]
	v_fmac_f32_e32 v203, v202, v135
	v_pk_mul_f32 v[208:209], v[208:209], s[56:57]
	v_fmac_f32_e32 v205, v204, v136
	v_pk_mul_f32 v[218:219], v[218:219], s[56:57]
	v_fmac_f32_e32 v221, v220, v137
	v_fmac_f32_e32 v145, v144, v133
	v_lshl_add_u64 v[142:143], v[142:143], 0, v[178:179]
	v_cvt_pk_bf16_f32 v200, v201, v203
	v_cvt_pk_bf16_f32 v201, v205, v221
	v_fmac_f32_e32 v207, v206, v130
	v_fmac_f32_e32 v209, v208, v131
	v_fmac_f32_e32 v219, v218, v132
	v_cvt_pk_bf16_f32 v202, v207, v209
	v_cvt_pk_bf16_f32 v203, v219, v145
	global_store_dwordx4 v[142:143], v[200:203], off
	v_lshlrev_b32_e32 v145, 16, v138
	v_mov_b32_e32 v144, v58
	v_and_b32_e32 v201, 0xffff0000, v138
	v_mov_b32_e32 v200, v59
	v_lshlrev_b32_e32 v205, 16, v140
	v_and_b32_e32 v207, 0xffff0000, v140
	v_pk_mul_f32 v[218:219], v[144:145], s[56:57]
	v_mov_b32_e32 v204, v50
	v_pk_mul_f32 v[200:201], v[200:201], s[56:57]
	v_mov_b32_e32 v206, v51
	v_lshlrev_b32_e32 v203, 16, v139
	v_and_b32_e32 v139, 0xffff0000, v139
	v_fmac_f32_e32 v219, v218, v134
	v_pk_mul_f32 v[204:205], v[204:205], s[56:57]
	v_fmac_f32_e32 v201, v200, v135
	v_pk_mul_f32 v[134:135], v[206:207], s[56:57]
	v_mov_b32_e32 v202, v60
	v_mov_b32_e32 v138, v61
	v_lshlrev_b32_e32 v209, 16, v141
	v_and_b32_e32 v141, 0xffff0000, v141
	v_fmac_f32_e32 v205, v204, v130
	v_fmac_f32_e32 v135, v134, v131
	v_pk_mul_f32 v[130:131], v[202:203], s[56:57]
	v_mov_b32_e32 v208, v52
	v_pk_mul_f32 v[138:139], v[138:139], s[56:57]
	v_mov_b32_e32 v140, v53
	v_fmac_f32_e32 v131, v130, v136
	v_pk_mul_f32 v[202:203], v[208:209], s[56:57]
	v_fmac_f32_e32 v139, v138, v137
	v_pk_mul_f32 v[136:137], v[140:141], s[56:57]
	v_or_b32_e32 v138, 0x80, v186
	v_fmac_f32_e32 v203, v202, v132
	v_fmac_f32_e32 v137, v136, v133
	v_lshl_add_u64 v[132:133], s[62:63], 0, v[194:195]
	v_cvt_pk_bf16_f32 v130, v219, v201
	v_cvt_pk_bf16_f32 v131, v131, v139
	v_ashrrev_i32_e32 v139, 31, v138
	v_lshl_add_u64 v[144:145], v[132:133], 0, v[178:179]
	v_lshl_add_u64 v[140:141], v[138:139], 2, v[188:189]
	v_lshl_add_u64 v[186:187], s[6:7], 0, v[190:191]
	v_lshlrev_b64 v[138:139], 1, v[138:139]
	v_cvt_pk_bf16_f32 v132, v205, v135
	v_cvt_pk_bf16_f32 v133, v203, v137
	global_store_dwordx4 v[144:145], v[130:133], off
	v_lshl_add_u64 v[186:187], v[186:187], 0, v[138:139]
	global_load_dwordx4 v[130:133], v[140:141], off offset:16
	global_load_dwordx4 v[134:137], v[140:141], off
	v_lshl_add_u64 v[184:185], s[6:7], 0, v[184:185]
	global_load_dwordx4 v[186:189], v[186:187], off
	v_lshl_add_u64 v[184:185], v[184:185], 0, v[138:139]
	global_load_dwordx4 v[200:203], v[184:185], off
	v_lshl_add_u64 v[184:185], s[6:7], 0, v[192:193]
	v_lshl_add_u64 v[184:185], v[184:185], 0, v[138:139]
	global_load_dwordx4 v[190:193], v[184:185], off
	v_lshl_add_u64 v[184:185], s[6:7], 0, v[194:195]
	v_lshl_add_u64 v[184:185], v[184:185], 0, v[138:139]
	global_load_dwordx4 v[204:207], v[184:185], off
	v_mov_b32_e32 v184, v126
	v_mov_b32_e32 v194, v127
	v_mov_b32_e32 v208, v128
	v_mov_b32_e32 v218, v122
	v_mov_b32_e32 v220, v123
	v_mov_b32_e32 v222, v124
	s_waitcnt vmcnt(0)
	v_lshlrev_b32_e32 v185, 16, v186
	v_and_b32_e32 v195, 0xffff0000, v186
	v_lshlrev_b32_e32 v209, 16, v187
	v_and_b32_e32 v187, 0xffff0000, v187
	v_pk_mul_f32 v[184:185], v[184:185], s[56:57]
	v_mov_b32_e32 v186, v129
	v_lshlrev_b32_e32 v219, 16, v188
	v_and_b32_e32 v221, 0xffff0000, v188
	v_lshlrev_b32_e32 v223, 16, v189
	v_and_b32_e32 v189, 0xffff0000, v189
	v_fmac_f32_e32 v185, v184, v134
	v_pk_mul_f32 v[194:195], v[194:195], s[56:57]
	v_pk_mul_f32 v[208:209], v[208:209], s[56:57]
	v_pk_mul_f32 v[186:187], v[186:187], s[56:57]
	v_mov_b32_e32 v188, v125
	v_pk_mul_f32 v[218:219], v[218:219], s[56:57]
	v_fmac_f32_e32 v195, v194, v135
	v_pk_mul_f32 v[220:221], v[220:221], s[56:57]
	v_fmac_f32_e32 v209, v208, v136
	v_pk_mul_f32 v[222:223], v[222:223], s[56:57]
	v_fmac_f32_e32 v187, v186, v137
	v_pk_mul_f32 v[188:189], v[188:189], s[56:57]
	v_cvt_pk_bf16_f32 v184, v185, v195
	v_cvt_pk_bf16_f32 v185, v209, v187
	v_fmac_f32_e32 v219, v218, v130
	v_fmac_f32_e32 v221, v220, v131
	v_fmac_f32_e32 v223, v222, v132
	v_fmac_f32_e32 v189, v188, v133
	v_cvt_pk_bf16_f32 v186, v219, v221
	v_cvt_pk_bf16_f32 v187, v223, v189
	global_store_dwordx4 v[196:197], v[184:187], off offset:256
	v_lshlrev_b32_e32 v189, 16, v201
	v_and_b32_e32 v195, 0xffff0000, v201
	v_lshlrev_b32_e32 v185, 16, v200
	v_mov_b32_e32 v184, v110
	v_and_b32_e32 v187, 0xffff0000, v200
	v_pk_mul_f32 v[184:185], v[184:185], s[56:57]
	v_mov_b32_e32 v186, v111
	v_mov_b32_e32 v188, v112
	v_mov_b32_e32 v194, v113
	v_lshlrev_b32_e32 v197, 16, v202
	v_and_b32_e32 v201, 0xffff0000, v202
	v_lshlrev_b32_e32 v209, 16, v203
	v_and_b32_e32 v203, 0xffff0000, v203
	v_fmac_f32_e32 v185, v184, v134
	v_mov_b32_e32 v196, v106
	v_pk_mul_f32 v[186:187], v[186:187], s[56:57]
	v_mov_b32_e32 v200, v107
	v_pk_mul_f32 v[188:189], v[188:189], s[56:57]
	v_mov_b32_e32 v208, v108
	v_pk_mul_f32 v[194:195], v[194:195], s[56:57]
	v_mov_b32_e32 v202, v109
	v_pk_mul_f32 v[196:197], v[196:197], s[56:57]
	v_fmac_f32_e32 v187, v186, v135
	v_pk_mul_f32 v[200:201], v[200:201], s[56:57]
	v_fmac_f32_e32 v189, v188, v136
	v_pk_mul_f32 v[208:209], v[208:209], s[56:57]
	v_fmac_f32_e32 v195, v194, v137
	v_pk_mul_f32 v[202:203], v[202:203], s[56:57]
	v_cvt_pk_bf16_f32 v184, v185, v187
	v_cvt_pk_bf16_f32 v185, v189, v195
	v_fmac_f32_e32 v197, v196, v130
	v_fmac_f32_e32 v201, v200, v131
	v_fmac_f32_e32 v209, v208, v132
	v_fmac_f32_e32 v203, v202, v133
	v_cvt_pk_bf16_f32 v186, v197, v201
	v_cvt_pk_bf16_f32 v187, v209, v203
	global_store_dwordx4 v[198:199], v[184:187], off offset:256
	v_lshlrev_b32_e32 v189, 16, v191
	v_and_b32_e32 v191, 0xffff0000, v191
	v_lshlrev_b32_e32 v185, 16, v190
	v_mov_b32_e32 v184, v94
	v_and_b32_e32 v187, 0xffff0000, v190
	v_pk_mul_f32 v[184:185], v[184:185], s[56:57]
	v_mov_b32_e32 v186, v95
	v_mov_b32_e32 v188, v96
	v_mov_b32_e32 v190, v97
	v_lshlrev_b32_e32 v195, 16, v192
	v_and_b32_e32 v197, 0xffff0000, v192
	v_lshlrev_b32_e32 v199, 16, v193
	v_and_b32_e32 v193, 0xffff0000, v193
	v_fmac_f32_e32 v185, v184, v134
	v_mov_b32_e32 v194, v90
	v_pk_mul_f32 v[186:187], v[186:187], s[56:57]
	v_mov_b32_e32 v196, v91
	v_pk_mul_f32 v[188:189], v[188:189], s[56:57]
	v_mov_b32_e32 v198, v92
	v_pk_mul_f32 v[190:191], v[190:191], s[56:57]
	v_mov_b32_e32 v192, v93
	v_pk_mul_f32 v[194:195], v[194:195], s[56:57]
	v_fmac_f32_e32 v187, v186, v135
	v_pk_mul_f32 v[196:197], v[196:197], s[56:57]
	v_fmac_f32_e32 v189, v188, v136
	v_pk_mul_f32 v[198:199], v[198:199], s[56:57]
	v_fmac_f32_e32 v191, v190, v137
	v_pk_mul_f32 v[192:193], v[192:193], s[56:57]
	v_cvt_pk_bf16_f32 v184, v185, v187
	v_cvt_pk_bf16_f32 v185, v189, v191
	v_fmac_f32_e32 v195, v194, v130
	v_fmac_f32_e32 v197, v196, v131
	v_fmac_f32_e32 v199, v198, v132
	v_fmac_f32_e32 v193, v192, v133
	v_cvt_pk_bf16_f32 v186, v195, v197
	v_cvt_pk_bf16_f32 v187, v199, v193
	global_store_dwordx4 v[142:143], v[184:187], off offset:256
	v_lshlrev_b32_e32 v143, 16, v204
	v_mov_b32_e32 v142, v78
	v_and_b32_e32 v185, 0xffff0000, v204
	v_mov_b32_e32 v184, v79
	v_lshlrev_b32_e32 v191, 16, v206
	v_and_b32_e32 v193, 0xffff0000, v206
	v_pk_mul_f32 v[142:143], v[142:143], s[56:57]
	v_mov_b32_e32 v190, v74
	v_pk_mul_f32 v[184:185], v[184:185], s[56:57]
	v_mov_b32_e32 v192, v75
	v_lshlrev_b32_e32 v187, 16, v205
	v_and_b32_e32 v189, 0xffff0000, v205
	v_fmac_f32_e32 v143, v142, v134
	v_pk_mul_f32 v[190:191], v[190:191], s[56:57]
	v_fmac_f32_e32 v185, v184, v135
	v_pk_mul_f32 v[134:135], v[192:193], s[56:57]
	v_mov_b32_e32 v186, v80
	v_mov_b32_e32 v188, v81
	v_lshlrev_b32_e32 v195, 16, v207
	v_and_b32_e32 v197, 0xffff0000, v207
	v_fmac_f32_e32 v191, v190, v130
	v_fmac_f32_e32 v135, v134, v131
	v_pk_mul_f32 v[130:131], v[186:187], s[56:57]
	v_mov_b32_e32 v194, v76
	v_pk_mul_f32 v[188:189], v[188:189], s[56:57]
	v_mov_b32_e32 v196, v77
	v_fmac_f32_e32 v131, v130, v136
	v_pk_mul_f32 v[186:187], v[194:195], s[56:57]
	v_fmac_f32_e32 v189, v188, v137
	v_pk_mul_f32 v[136:137], v[196:197], s[56:57]
	v_fmac_f32_e32 v187, v186, v132
	v_fmac_f32_e32 v137, v136, v133
	v_cvt_pk_bf16_f32 v130, v143, v185
	v_cvt_pk_bf16_f32 v131, v131, v189
	v_cvt_pk_bf16_f32 v132, v191, v135
	v_cvt_pk_bf16_f32 v133, v187, v137
	global_store_dwordx4 v[144:145], v[130:133], off offset:256
	v_ashrrev_i32_e32 v143, 31, v169
	v_mov_b32_e32 v142, v169
	global_load_dwordx4 v[130:133], v[182:183], off offset:16
	global_load_dwordx4 v[134:137], v[182:183], off
	v_lshlrev_b64 v[182:183], 12, v[142:143]
	v_lshl_add_u64 v[142:143], v[180:181], 0, v[182:183]
	global_load_dwordx4 v[188:191], v[142:143], off
	v_ashrrev_i32_e32 v143, 31, v167
	v_mov_b32_e32 v142, v167
	v_lshlrev_b64 v[142:143], 12, v[142:143]
	v_lshl_add_u64 v[144:145], v[180:181], 0, v[142:143]
	global_load_dwordx4 v[192:195], v[144:145], off
	v_ashrrev_i32_e32 v145, 31, v165
	v_mov_b32_e32 v144, v165
	v_lshlrev_b64 v[144:145], 12, v[144:145]
	v_lshl_add_u64 v[184:185], v[180:181], 0, v[144:145]
	global_load_dwordx4 v[196:199], v[184:185], off
	v_ashrrev_i32_e32 v185, 31, v161
	v_mov_b32_e32 v184, v161
	v_lshlrev_b64 v[186:187], 12, v[184:185]
	v_lshl_add_u64 v[180:181], v[180:181], 0, v[186:187]
	global_load_dwordx4 v[200:203], v[180:181], off
	v_mov_b32_e32 v180, v70
	v_mov_b32_e32 v206, v62
	v_mov_b32_e32 v184, v71
	v_mov_b32_e32 v208, v63
	v_mov_b32_e32 v204, v72
	v_mov_b32_e32 v218, v64
	s_waitcnt vmcnt(0)
	v_lshlrev_b32_e32 v181, 16, v188
	v_and_b32_e32 v185, 0xffff0000, v188
	v_lshlrev_b32_e32 v205, 16, v189
	v_and_b32_e32 v189, 0xffff0000, v189
	v_lshlrev_b32_e32 v207, 16, v190
	v_and_b32_e32 v209, 0xffff0000, v190
	v_lshlrev_b32_e32 v219, 16, v191
	v_and_b32_e32 v191, 0xffff0000, v191
	v_mov_b32_e32 v188, v73
	v_mov_b32_e32 v190, v65
	v_pk_mul_f32 v[188:189], v[188:189], s[56:57]
	v_pk_mul_f32 v[190:191], v[190:191], s[56:57]
	v_pk_mul_f32 v[220:221], v[180:181], s[56:57]
	v_pk_mul_f32 v[206:207], v[206:207], s[56:57]
	v_pk_mul_f32 v[184:185], v[184:185], s[56:57]
	v_pk_mul_f32 v[208:209], v[208:209], s[56:57]
	v_pk_mul_f32 v[204:205], v[204:205], s[56:57]
	v_pk_mul_f32 v[218:219], v[218:219], s[56:57]
	v_fmac_f32_e32 v189, v188, v137
	v_fmac_f32_e32 v191, v190, v133
	v_lshl_add_u64 v[180:181], s[62:63], 0, v[182:183]
	v_fmac_f32_e32 v221, v220, v134
	v_fmac_f32_e32 v207, v206, v130
	v_fmac_f32_e32 v185, v184, v135
	v_fmac_f32_e32 v209, v208, v131
	v_fmac_f32_e32 v205, v204, v136
	v_fmac_f32_e32 v219, v218, v132
	v_lshl_add_u64 v[180:181], v[180:181], 0, v[178:179]
	v_cvt_pk_bf16_f32 v188, v221, v185
	v_cvt_pk_bf16_f32 v189, v205, v189
	v_cvt_pk_bf16_f32 v190, v207, v209
	v_cvt_pk_bf16_f32 v191, v219, v191
	global_store_dwordx4 v[180:181], v[188:191], off
	v_lshlrev_b32_e32 v185, 16, v192
	v_lshlrev_b32_e32 v205, 16, v194
	v_and_b32_e32 v189, 0xffff0000, v192
	v_lshlrev_b32_e32 v191, 16, v193
	v_mov_b32_e32 v188, v47
	v_mov_b32_e32 v190, v48
	v_and_b32_e32 v193, 0xffff0000, v193
	v_and_b32_e32 v207, 0xffff0000, v194
	v_lshlrev_b32_e32 v209, 16, v195
	v_and_b32_e32 v195, 0xffff0000, v195
	v_mov_b32_e32 v184, v46
	v_mov_b32_e32 v204, v38
	v_pk_mul_f32 v[188:189], v[188:189], s[56:57]
	v_mov_b32_e32 v206, v39
	v_pk_mul_f32 v[190:191], v[190:191], s[56:57]
	v_mov_b32_e32 v208, v40
	v_mov_b32_e32 v192, v49
	v_mov_b32_e32 v194, v41
	v_pk_mul_f32 v[218:219], v[184:185], s[56:57]
	v_pk_mul_f32 v[204:205], v[204:205], s[56:57]
	v_fmac_f32_e32 v189, v188, v135
	v_pk_mul_f32 v[206:207], v[206:207], s[56:57]
	v_fmac_f32_e32 v191, v190, v136
	v_pk_mul_f32 v[208:209], v[208:209], s[56:57]
	v_pk_mul_f32 v[192:193], v[192:193], s[56:57]
	v_pk_mul_f32 v[194:195], v[194:195], s[56:57]
	v_lshl_add_u64 v[184:185], s[62:63], 0, v[142:143]
	v_fmac_f32_e32 v219, v218, v134
	v_fmac_f32_e32 v205, v204, v130
	v_fmac_f32_e32 v207, v206, v131
	v_fmac_f32_e32 v209, v208, v132
	v_fmac_f32_e32 v193, v192, v137
	v_fmac_f32_e32 v195, v194, v133
	v_lshl_add_u64 v[184:185], v[184:185], 0, v[178:179]
	v_cvt_pk_bf16_f32 v188, v219, v189
	v_cvt_pk_bf16_f32 v189, v191, v193
	v_cvt_pk_bf16_f32 v190, v205, v207
	v_cvt_pk_bf16_f32 v191, v209, v195
	global_store_dwordx4 v[184:185], v[188:191], off
	v_lshlrev_b32_e32 v193, 16, v197
	v_mov_b32_e32 v192, v32
	v_and_b32_e32 v191, 0xffff0000, v196
	v_mov_b32_e32 v190, v31
	v_lshlrev_b32_e32 v189, 16, v196
	v_and_b32_e32 v195, 0xffff0000, v197
	v_lshlrev_b32_e32 v197, 16, v198
	v_and_b32_e32 v205, 0xffff0000, v198
	v_lshlrev_b32_e32 v207, 16, v199
	v_and_b32_e32 v199, 0xffff0000, v199
	v_mov_b32_e32 v188, v30
	v_mov_b32_e32 v196, v22
	v_pk_mul_f32 v[190:191], v[190:191], s[56:57]
	v_mov_b32_e32 v204, v23
	v_pk_mul_f32 v[192:193], v[192:193], s[56:57]
	v_mov_b32_e32 v206, v24
	v_mov_b32_e32 v194, v33
	v_mov_b32_e32 v198, v25
	v_pk_mul_f32 v[208:209], v[188:189], s[56:57]
	v_pk_mul_f32 v[196:197], v[196:197], s[56:57]
	v_fmac_f32_e32 v191, v190, v135
	v_pk_mul_f32 v[204:205], v[204:205], s[56:57]
	v_fmac_f32_e32 v193, v192, v136
	v_pk_mul_f32 v[206:207], v[206:207], s[56:57]
	v_pk_mul_f32 v[194:195], v[194:195], s[56:57]
	v_pk_mul_f32 v[198:199], v[198:199], s[56:57]
	v_lshl_add_u64 v[188:189], s[62:63], 0, v[144:145]
	v_fmac_f32_e32 v209, v208, v134
	v_fmac_f32_e32 v197, v196, v130
	v_fmac_f32_e32 v205, v204, v131
	v_fmac_f32_e32 v207, v206, v132
	v_fmac_f32_e32 v195, v194, v137
	v_fmac_f32_e32 v199, v198, v133
	v_lshl_add_u64 v[188:189], v[188:189], 0, v[178:179]
	v_cvt_pk_bf16_f32 v190, v209, v191
	v_cvt_pk_bf16_f32 v191, v193, v195
	v_cvt_pk_bf16_f32 v192, v197, v205
	v_cvt_pk_bf16_f32 v193, v207, v199
	global_store_dwordx4 v[188:189], v[190:193], off
	v_lshlrev_b32_e32 v195, 16, v201
	v_and_b32_e32 v197, 0xffff0000, v201
	v_lshlrev_b32_e32 v191, 16, v200
	v_and_b32_e32 v193, 0xffff0000, v200
	v_mov_b32_e32 v190, v14
	v_mov_b32_e32 v192, v15
	v_lshlrev_b32_e32 v199, 16, v202
	v_and_b32_e32 v201, 0xffff0000, v202
	v_pk_mul_f32 v[190:191], v[190:191], s[56:57]
	v_mov_b32_e32 v198, v6
	v_pk_mul_f32 v[192:193], v[192:193], s[56:57]
	v_mov_b32_e32 v200, v7
	v_fmac_f32_e32 v191, v190, v134
	v_pk_mul_f32 v[198:199], v[198:199], s[56:57]
	v_fmac_f32_e32 v193, v192, v135
	v_pk_mul_f32 v[134:135], v[200:201], s[56:57]
	v_mov_b32_e32 v194, v16
	v_mov_b32_e32 v196, v17
	v_lshlrev_b32_e32 v205, 16, v203
	v_and_b32_e32 v203, 0xffff0000, v203
	v_fmac_f32_e32 v199, v198, v130
	v_fmac_f32_e32 v135, v134, v131
	v_pk_mul_f32 v[130:131], v[194:195], s[56:57]
	v_mov_b32_e32 v204, v8
	v_pk_mul_f32 v[196:197], v[196:197], s[56:57]
	v_mov_b32_e32 v202, v9
	v_fmac_f32_e32 v131, v130, v136
	v_pk_mul_f32 v[194:195], v[204:205], s[56:57]
	v_fmac_f32_e32 v197, v196, v137
	v_pk_mul_f32 v[136:137], v[202:203], s[56:57]
	v_fmac_f32_e32 v195, v194, v132
	v_fmac_f32_e32 v137, v136, v133
	v_lshl_add_u64 v[132:133], s[62:63], 0, v[186:187]
	v_lshl_add_u64 v[178:179], v[132:133], 0, v[178:179]
	v_cvt_pk_bf16_f32 v130, v191, v193
	v_cvt_pk_bf16_f32 v131, v131, v197
	v_cvt_pk_bf16_f32 v132, v199, v135
	v_cvt_pk_bf16_f32 v133, v195, v137
	global_store_dwordx4 v[178:179], v[130:133], off
	global_load_dwordx4 v[130:133], v[140:141], off offset:16
	s_nop 0
	global_load_dwordx4 v[134:137], v[140:141], off
	v_lshl_add_u64 v[140:141], s[6:7], 0, v[182:183]
	v_lshl_add_u64 v[140:141], v[140:141], 0, v[138:139]
	v_lshl_add_u64 v[144:145], s[6:7], 0, v[144:145]
	global_load_dwordx4 v[190:193], v[140:141], off
	v_lshl_add_u64 v[144:145], v[144:145], 0, v[138:139]
	global_load_dwordx4 v[194:197], v[144:145], off
	v_lshl_add_u64 v[140:141], s[6:7], 0, v[142:143]
	v_lshl_add_u64 v[140:141], v[140:141], 0, v[138:139]
	global_load_dwordx4 v[140:143], v[140:141], off
	v_lshl_add_u64 v[144:145], s[6:7], 0, v[186:187]
	v_lshl_add_u64 v[138:139], v[144:145], 0, v[138:139]
	global_load_dwordx4 v[198:201], v[138:139], off
	v_mov_b32_e32 v138, v66
	v_mov_b32_e32 v144, v67
	v_mov_b32_e32 v202, v55
	v_mov_b32_e32 v182, v68
	v_mov_b32_e32 v204, v56
	v_mov_b32_e32 v186, v69
	s_waitcnt vmcnt(0)
	v_lshlrev_b32_e32 v139, 16, v190
	v_and_b32_e32 v145, 0xffff0000, v190
	v_lshlrev_b32_e32 v183, 16, v191
	v_and_b32_e32 v187, 0xffff0000, v191
	v_lshlrev_b32_e32 v191, 16, v192
	v_and_b32_e32 v203, 0xffff0000, v192
	v_lshlrev_b32_e32 v205, 16, v193
	v_and_b32_e32 v193, 0xffff0000, v193
	v_mov_b32_e32 v192, v57
	v_pk_mul_f32 v[138:139], v[138:139], s[56:57]
	v_mov_b32_e32 v190, v54
	v_pk_mul_f32 v[144:145], v[144:145], s[56:57]
	v_pk_mul_f32 v[192:193], v[192:193], s[56:57]
	v_fmac_f32_e32 v139, v138, v134
	v_pk_mul_f32 v[206:207], v[190:191], s[56:57]
	v_fmac_f32_e32 v145, v144, v135
	v_pk_mul_f32 v[202:203], v[202:203], s[56:57]
	v_pk_mul_f32 v[182:183], v[182:183], s[56:57]
	v_pk_mul_f32 v[204:205], v[204:205], s[56:57]
	v_pk_mul_f32 v[186:187], v[186:187], s[56:57]
	v_fmac_f32_e32 v193, v192, v133
	v_fmac_f32_e32 v207, v206, v130
	v_fmac_f32_e32 v203, v202, v131
	v_fmac_f32_e32 v183, v182, v136
	v_fmac_f32_e32 v205, v204, v132
	v_fmac_f32_e32 v187, v186, v137
	v_cvt_pk_bf16_f32 v190, v139, v145
	v_cvt_pk_bf16_f32 v191, v183, v187
	v_cvt_pk_bf16_f32 v192, v207, v203
	v_cvt_pk_bf16_f32 v193, v205, v193
	global_store_dwordx4 v[180:181], v[190:193], off offset:256
	v_lshlrev_b32_e32 v139, 16, v140
	v_and_b32_e32 v145, 0xffff0000, v140
	v_lshlrev_b32_e32 v181, 16, v141
	v_and_b32_e32 v141, 0xffff0000, v141
	v_mov_b32_e32 v138, v42
	v_mov_b32_e32 v140, v45
	v_lshlrev_b32_e32 v183, 16, v142
	v_and_b32_e32 v187, 0xffff0000, v142
	v_lshlrev_b32_e32 v191, 16, v143
	v_and_b32_e32 v143, 0xffff0000, v143
	v_pk_mul_f32 v[138:139], v[138:139], s[56:57]
	v_mov_b32_e32 v182, v34
	v_mov_b32_e32 v144, v43
	v_mov_b32_e32 v186, v35
	v_mov_b32_e32 v180, v44
	v_mov_b32_e32 v190, v36
	v_pk_mul_f32 v[140:141], v[140:141], s[56:57]
	v_mov_b32_e32 v142, v37
	v_fmac_f32_e32 v139, v138, v134
	v_pk_mul_f32 v[182:183], v[182:183], s[56:57]
	v_pk_mul_f32 v[144:145], v[144:145], s[56:57]
	v_pk_mul_f32 v[186:187], v[186:187], s[56:57]
	v_pk_mul_f32 v[180:181], v[180:181], s[56:57]
	v_pk_mul_f32 v[190:191], v[190:191], s[56:57]
	v_fmac_f32_e32 v141, v140, v137
	v_pk_mul_f32 v[142:143], v[142:143], s[56:57]
	v_fmac_f32_e32 v183, v182, v130
	v_fmac_f32_e32 v145, v144, v135
	v_fmac_f32_e32 v187, v186, v131
	v_fmac_f32_e32 v181, v180, v136
	v_fmac_f32_e32 v191, v190, v132
	v_fmac_f32_e32 v143, v142, v133
	v_cvt_pk_bf16_f32 v138, v139, v145
	v_cvt_pk_bf16_f32 v139, v181, v141
	v_cvt_pk_bf16_f32 v140, v183, v187
	v_cvt_pk_bf16_f32 v141, v191, v143
	global_store_dwordx4 v[184:185], v[138:141], off offset:256
	v_lshlrev_b32_e32 v143, 16, v195
	v_and_b32_e32 v145, 0xffff0000, v195
	v_lshlrev_b32_e32 v139, 16, v194
	v_and_b32_e32 v141, 0xffff0000, v194
	v_mov_b32_e32 v138, v26
	v_mov_b32_e32 v140, v27
	v_lshlrev_b32_e32 v181, 16, v196
	v_and_b32_e32 v183, 0xffff0000, v196
	v_lshlrev_b32_e32 v185, 16, v197
	v_and_b32_e32 v187, 0xffff0000, v197
	v_pk_mul_f32 v[138:139], v[138:139], s[56:57]
	v_mov_b32_e32 v180, v18
	v_pk_mul_f32 v[140:141], v[140:141], s[56:57]
	v_mov_b32_e32 v182, v19
	v_mov_b32_e32 v142, v28
	v_mov_b32_e32 v184, v20
	v_mov_b32_e32 v144, v29
	v_mov_b32_e32 v186, v21
	v_fmac_f32_e32 v139, v138, v134
	v_pk_mul_f32 v[180:181], v[180:181], s[56:57]
	v_fmac_f32_e32 v141, v140, v135
	v_pk_mul_f32 v[182:183], v[182:183], s[56:57]
	v_pk_mul_f32 v[142:143], v[142:143], s[56:57]
	v_pk_mul_f32 v[184:185], v[184:185], s[56:57]
	v_pk_mul_f32 v[144:145], v[144:145], s[56:57]
	v_pk_mul_f32 v[186:187], v[186:187], s[56:57]
	v_fmac_f32_e32 v181, v180, v130
	v_fmac_f32_e32 v183, v182, v131
	v_fmac_f32_e32 v143, v142, v136
	v_fmac_f32_e32 v185, v184, v132
	v_fmac_f32_e32 v145, v144, v137
	v_fmac_f32_e32 v187, v186, v133
	v_cvt_pk_bf16_f32 v138, v139, v141
	v_cvt_pk_bf16_f32 v139, v143, v145
	v_cvt_pk_bf16_f32 v140, v181, v183
	v_cvt_pk_bf16_f32 v141, v185, v187
	global_store_dwordx4 v[188:189], v[138:141], off offset:256
	v_lshlrev_b32_e32 v181, 16, v200
	v_and_b32_e32 v183, 0xffff0000, v200
	v_lshlrev_b32_e32 v139, 16, v198
	v_and_b32_e32 v141, 0xffff0000, v198
	v_mov_b32_e32 v138, v10
	v_mov_b32_e32 v140, v11
	v_pk_mul_f32 v[138:139], v[138:139], s[56:57]
	v_mov_b32_e32 v180, v2
	v_pk_mul_f32 v[140:141], v[140:141], s[56:57]
	v_mov_b32_e32 v182, v3
	v_lshlrev_b32_e32 v143, 16, v199
	v_and_b32_e32 v145, 0xffff0000, v199
	v_fmac_f32_e32 v139, v138, v134
	v_pk_mul_f32 v[180:181], v[180:181], s[56:57]
	v_fmac_f32_e32 v141, v140, v135
	v_pk_mul_f32 v[134:135], v[182:183], s[56:57]
	v_mov_b32_e32 v142, v12
	v_mov_b32_e32 v144, v13
	v_lshlrev_b32_e32 v185, 16, v201
	v_and_b32_e32 v187, 0xffff0000, v201
	v_fmac_f32_e32 v181, v180, v130
	v_fmac_f32_e32 v135, v134, v131
	v_pk_mul_f32 v[130:131], v[142:143], s[56:57]
	v_mov_b32_e32 v184, v4
	v_pk_mul_f32 v[144:145], v[144:145], s[56:57]
	v_mov_b32_e32 v186, v5
	v_fmac_f32_e32 v131, v130, v136
	v_pk_mul_f32 v[142:143], v[184:185], s[56:57]
	v_fmac_f32_e32 v145, v144, v137
	v_pk_mul_f32 v[136:137], v[186:187], s[56:57]
	v_fmac_f32_e32 v143, v142, v132
	v_fmac_f32_e32 v137, v136, v133
	v_cvt_pk_bf16_f32 v130, v139, v141
	v_cvt_pk_bf16_f32 v131, v131, v145
	v_cvt_pk_bf16_f32 v132, v181, v135
	v_cvt_pk_bf16_f32 v133, v143, v137
	global_store_dwordx4 v[178:179], v[130:133], off offset:256
